# speedup vs baseline: 1.0220x; 1.0009x over previous
.Lou_loop:
	s_waitcnt lgkmcnt(0)
	v_mfma_f32_16x16x32_bf16 v[64:67], v[176:179], v[160:163], v[64:67]
	ds_read_b128 v[200:203], v11 offset:0
	v_mfma_f32_16x16x32_bf16 v[68:71], v[176:179], v[164:167], v[68:71]
	s_add_u32 m0, s20, 0x5000
	v_mfma_f32_16x16x32_bf16 v[72:75], v[176:179], v[168:171], v[72:75]
	ds_read_b128 v[204:207], v11 offset:2048
	v_mfma_f32_16x16x32_bf16 v[76:79], v[176:179], v[172:175], v[76:79]
	global_load_lds_dwordx4 v3, s[18:19]
	v_mfma_f32_16x16x32_bf16 v[80:83], v[180:183], v[160:163], v[80:83]
	ds_read_b128 v[208:211], v11 offset:4096
	v_mfma_f32_16x16x32_bf16 v[84:87], v[180:183], v[164:167], v[84:87]
	s_add_u32 m0, s20, 0x6000
	v_mfma_f32_16x16x32_bf16 v[88:91], v[180:183], v[168:171], v[88:91]
	ds_read_b128 v[212:215], v11 offset:6144
	v_mfma_f32_16x16x32_bf16 v[92:95], v[180:183], v[172:175], v[92:95]
	global_load_lds_dwordx4 v4, s[18:19]
	v_mfma_f32_16x16x32_bf16 v[96:99], v[184:187], v[160:163], v[96:99]
	ds_read_b128 v[216:219], v13 offset:0
	v_mfma_f32_16x16x32_bf16 v[100:103], v[184:187], v[164:167], v[100:103]
	s_add_u32 m0, s20, 0x7000
	v_mfma_f32_16x16x32_bf16 v[104:107], v[184:187], v[168:171], v[104:107]
	ds_read_b128 v[220:223], v13 offset:2048
	v_mfma_f32_16x16x32_bf16 v[108:111], v[184:187], v[172:175], v[108:111]
	global_load_lds_dwordx4 v5, s[18:19]
	v_mfma_f32_16x16x32_bf16 v[112:115], v[188:191], v[160:163], v[112:115]
	ds_read_b128 v[224:227], v13 offset:4096
	v_mfma_f32_16x16x32_bf16 v[116:119], v[188:191], v[164:167], v[116:119]
	s_add_u32 m0, s20, 0x8000
	v_mfma_f32_16x16x32_bf16 v[120:123], v[188:191], v[168:171], v[120:123]
	ds_read_b128 v[228:231], v13 offset:6144
	v_mfma_f32_16x16x32_bf16 v[124:127], v[188:191], v[172:175], v[124:127]
	global_load_lds_dwordx4 v6, s[18:19]
	v_mfma_f32_16x16x32_bf16 v[128:131], v[192:195], v[160:163], v[128:131]
	ds_read_b128 v[232:235], v13 offset:8192
	v_mfma_f32_16x16x32_bf16 v[132:135], v[192:195], v[164:167], v[132:135]
	s_add_u32 m0, s20, 0x9000
	v_mfma_f32_16x16x32_bf16 v[136:139], v[192:195], v[168:171], v[136:139]
	ds_read_b128 v[236:239], v13 offset:10240
	v_mfma_f32_16x16x32_bf16 v[140:143], v[192:195], v[172:175], v[140:143]
	global_load_lds_dwordx4 v7, s[18:19]
	v_mfma_f32_16x16x32_bf16 v[144:147], v[196:199], v[160:163], v[144:147]
	s_add_u32 s16, s16, 0x80
	s_addc_u32 s17, s17, 0
	s_add_u32 s18, s18, 0x80
	s_addc_u32 s19, s19, 0
	v_mfma_f32_16x16x32_bf16 v[148:151], v[196:199], v[164:167], v[148:151]
	s_add_u32 s20, s20, 0xa000
	s_sub_u32 s22, s20, 0x28000
	s_cmp_ge_u32 s20, 0x28000
	s_cselect_b32 s20, s22, s20
	v_mfma_f32_16x16x32_bf16 v[152:155], v[196:199], v[168:171], v[152:155]
	v_add_u32_e32 v10, s21, v8
	v_add_u32_e32 v12, s21, v9
	v_xor_b32_e32 v11, 64, v10
	v_xor_b32_e32 v13, 64, v12
	v_mfma_f32_16x16x32_bf16 v[156:159], v[196:199], v[172:175], v[156:159]
	s_add_u32 s21, s21, 0xa000
	s_sub_u32 s23, s21, 0x28000
	s_cmp_ge_u32 s21, 0x28000
	s_cselect_b32 s21, s23, s21
	s_waitcnt vmcnt(20) lgkmcnt(0)
	s_barrier
	v_mfma_f32_16x16x32_bf16 v[64:67], v[216:219], v[200:203], v[64:67]
	ds_read_b128 v[160:163], v10 offset:0
	v_mfma_f32_16x16x32_bf16 v[68:71], v[216:219], v[204:207], v[68:71]
	s_add_u32 m0, s20, 0x0
	v_mfma_f32_16x16x32_bf16 v[72:75], v[216:219], v[208:211], v[72:75]
	ds_read_b128 v[164:167], v10 offset:2048
	v_mfma_f32_16x16x32_bf16 v[76:79], v[216:219], v[212:215], v[76:79]
	global_load_lds_dwordx4 v2, s[16:17]
	v_mfma_f32_16x16x32_bf16 v[80:83], v[220:223], v[200:203], v[80:83]
	ds_read_b128 v[168:171], v10 offset:4096
	v_mfma_f32_16x16x32_bf16 v[84:87], v[220:223], v[204:207], v[84:87]
	s_add_u32 m0, s20, 0x1000
	v_mfma_f32_16x16x32_bf16 v[88:91], v[220:223], v[208:211], v[88:91]
	ds_read_b128 v[172:175], v10 offset:6144
	v_mfma_f32_16x16x32_bf16 v[92:95], v[220:223], v[212:215], v[92:95]
	global_load_lds_dwordx4 v3, s[16:17]
	v_mfma_f32_16x16x32_bf16 v[96:99], v[224:227], v[200:203], v[96:99]
	ds_read_b128 v[176:179], v12 offset:0
	v_mfma_f32_16x16x32_bf16 v[100:103], v[224:227], v[204:207], v[100:103]
	s_add_u32 m0, s20, 0x2000
	v_mfma_f32_16x16x32_bf16 v[104:107], v[224:227], v[208:211], v[104:107]
	ds_read_b128 v[180:183], v12 offset:2048
	v_mfma_f32_16x16x32_bf16 v[108:111], v[224:227], v[212:215], v[108:111]
	global_load_lds_dwordx4 v4, s[16:17]
	v_mfma_f32_16x16x32_bf16 v[112:115], v[228:231], v[200:203], v[112:115]
	ds_read_b128 v[184:187], v12 offset:4096
	v_mfma_f32_16x16x32_bf16 v[116:119], v[228:231], v[204:207], v[116:119]
	s_add_u32 m0, s20, 0x3000
	v_mfma_f32_16x16x32_bf16 v[120:123], v[228:231], v[208:211], v[120:123]
	ds_read_b128 v[188:191], v12 offset:6144
	v_mfma_f32_16x16x32_bf16 v[124:127], v[228:231], v[212:215], v[124:127]
	global_load_lds_dwordx4 v5, s[16:17]
	v_mfma_f32_16x16x32_bf16 v[128:131], v[232:235], v[200:203], v[128:131]
	ds_read_b128 v[192:195], v12 offset:8192
	v_mfma_f32_16x16x32_bf16 v[132:135], v[232:235], v[204:207], v[132:135]
	s_add_u32 m0, s20, 0x4000
	v_mfma_f32_16x16x32_bf16 v[136:139], v[232:235], v[208:211], v[136:139]
	ds_read_b128 v[196:199], v12 offset:10240
	v_mfma_f32_16x16x32_bf16 v[140:143], v[232:235], v[212:215], v[140:143]
	global_load_lds_dwordx4 v2, s[18:19]
	v_mfma_f32_16x16x32_bf16 v[144:147], v[236:239], v[200:203], v[144:147]
	v_mfma_f32_16x16x32_bf16 v[148:151], v[236:239], v[204:207], v[148:151]
	v_mfma_f32_16x16x32_bf16 v[152:155], v[236:239], v[208:211], v[152:155]
	v_mfma_f32_16x16x32_bf16 v[156:159], v[236:239], v[212:215], v[156:159]
	s_add_u32 s15, s15, 1
	s_cmp_lt_u32 s15, 8
	s_cbranch_scc1 .Lou_loop
	s_waitcnt lgkmcnt(0)
	v_mfma_f32_16x16x32_bf16 v[64:67], v[176:179], v[160:163], v[64:67]
	ds_read_b128 v[200:203], v11 offset:0
	v_mfma_f32_16x16x32_bf16 v[68:71], v[176:179], v[164:167], v[68:71]
	s_add_u32 m0, s20, 0x5000
	v_mfma_f32_16x16x32_bf16 v[72:75], v[176:179], v[168:171], v[72:75]
	ds_read_b128 v[204:207], v11 offset:2048
	v_mfma_f32_16x16x32_bf16 v[76:79], v[176:179], v[172:175], v[76:79]
	global_load_lds_dwordx4 v3, s[18:19]
	v_mfma_f32_16x16x32_bf16 v[80:83], v[180:183], v[160:163], v[80:83]
	ds_read_b128 v[208:211], v11 offset:4096
	v_mfma_f32_16x16x32_bf16 v[84:87], v[180:183], v[164:167], v[84:87]
	s_add_u32 m0, s20, 0x6000
	v_mfma_f32_16x16x32_bf16 v[88:91], v[180:183], v[168:171], v[88:91]
	ds_read_b128 v[212:215], v11 offset:6144
	v_mfma_f32_16x16x32_bf16 v[92:95], v[180:183], v[172:175], v[92:95]
	global_load_lds_dwordx4 v4, s[18:19]
	v_mfma_f32_16x16x32_bf16 v[96:99], v[184:187], v[160:163], v[96:99]
	ds_read_b128 v[216:219], v13 offset:0
	v_mfma_f32_16x16x32_bf16 v[100:103], v[184:187], v[164:167], v[100:103]
	s_add_u32 m0, s20, 0x7000
	v_mfma_f32_16x16x32_bf16 v[104:107], v[184:187], v[168:171], v[104:107]
	ds_read_b128 v[220:223], v13 offset:2048
	v_mfma_f32_16x16x32_bf16 v[108:111], v[184:187], v[172:175], v[108:111]
	global_load_lds_dwordx4 v5, s[18:19]
	v_mfma_f32_16x16x32_bf16 v[112:115], v[188:191], v[160:163], v[112:115]
	ds_read_b128 v[224:227], v13 offset:4096
	v_mfma_f32_16x16x32_bf16 v[116:119], v[188:191], v[164:167], v[116:119]
	s_add_u32 m0, s20, 0x8000
	v_mfma_f32_16x16x32_bf16 v[120:123], v[188:191], v[168:171], v[120:123]
	ds_read_b128 v[228:231], v13 offset:6144
	v_mfma_f32_16x16x32_bf16 v[124:127], v[188:191], v[172:175], v[124:127]
	global_load_lds_dwordx4 v6, s[18:19]
	v_mfma_f32_16x16x32_bf16 v[128:131], v[192:195], v[160:163], v[128:131]
	ds_read_b128 v[232:235], v13 offset:8192
	v_mfma_f32_16x16x32_bf16 v[132:135], v[192:195], v[164:167], v[132:135]
	s_add_u32 m0, s20, 0x9000
	v_mfma_f32_16x16x32_bf16 v[136:139], v[192:195], v[168:171], v[136:139]
	ds_read_b128 v[236:239], v13 offset:10240
	v_mfma_f32_16x16x32_bf16 v[140:143], v[192:195], v[172:175], v[140:143]
	global_load_lds_dwordx4 v7, s[18:19]
	v_mfma_f32_16x16x32_bf16 v[144:147], v[196:199], v[160:163], v[144:147]
	s_add_u32 s16, s16, 0x80
	s_addc_u32 s17, s17, 0
	s_add_u32 s18, s18, 0x80
	s_addc_u32 s19, s19, 0
	v_mfma_f32_16x16x32_bf16 v[148:151], v[196:199], v[164:167], v[148:151]
	s_add_u32 s20, s20, 0xa000
	s_sub_u32 s22, s20, 0x28000
	s_cmp_ge_u32 s20, 0x28000
	s_cselect_b32 s20, s22, s20
	v_mfma_f32_16x16x32_bf16 v[152:155], v[196:199], v[168:171], v[152:155]
	v_add_u32_e32 v10, s21, v8
	v_add_u32_e32 v12, s21, v9
	v_xor_b32_e32 v11, 64, v10
	v_xor_b32_e32 v13, 64, v12
	v_mfma_f32_16x16x32_bf16 v[156:159], v[196:199], v[172:175], v[156:159]
	s_add_u32 s21, s21, 0xa000
	s_sub_u32 s23, s21, 0x28000
	s_cmp_ge_u32 s21, 0x28000
	s_cselect_b32 s21, s23, s21
	s_waitcnt vmcnt(20) lgkmcnt(0)
	s_barrier
	v_mfma_f32_16x16x32_bf16 v[64:67], v[216:219], v[200:203], v[64:67]
	ds_read_b128 v[160:163], v10 offset:0
	v_mfma_f32_16x16x32_bf16 v[68:71], v[216:219], v[204:207], v[68:71]
	ds_read_b128 v[164:167], v10 offset:2048
	v_mfma_f32_16x16x32_bf16 v[72:75], v[216:219], v[208:211], v[72:75]
	ds_read_b128 v[168:171], v10 offset:4096
	v_mfma_f32_16x16x32_bf16 v[76:79], v[216:219], v[212:215], v[76:79]
	ds_read_b128 v[172:175], v10 offset:6144
	v_mfma_f32_16x16x32_bf16 v[80:83], v[220:223], v[200:203], v[80:83]
	ds_read_b128 v[176:179], v12 offset:0
	v_mfma_f32_16x16x32_bf16 v[84:87], v[220:223], v[204:207], v[84:87]
	ds_read_b128 v[180:183], v12 offset:2048
	v_mfma_f32_16x16x32_bf16 v[88:91], v[220:223], v[208:211], v[88:91]
	ds_read_b128 v[184:187], v12 offset:4096
	v_mfma_f32_16x16x32_bf16 v[92:95], v[220:223], v[212:215], v[92:95]
	ds_read_b128 v[188:191], v12 offset:6144
	v_mfma_f32_16x16x32_bf16 v[96:99], v[224:227], v[200:203], v[96:99]
	ds_read_b128 v[192:195], v12 offset:8192
	v_mfma_f32_16x16x32_bf16 v[100:103], v[224:227], v[204:207], v[100:103]
	ds_read_b128 v[196:199], v12 offset:10240
	v_mfma_f32_16x16x32_bf16 v[104:107], v[224:227], v[208:211], v[104:107]
	v_mfma_f32_16x16x32_bf16 v[108:111], v[224:227], v[212:215], v[108:111]
	v_mfma_f32_16x16x32_bf16 v[112:115], v[228:231], v[200:203], v[112:115]
	v_mfma_f32_16x16x32_bf16 v[116:119], v[228:231], v[204:207], v[116:119]
	v_mfma_f32_16x16x32_bf16 v[120:123], v[228:231], v[208:211], v[120:123]
	v_mfma_f32_16x16x32_bf16 v[124:127], v[228:231], v[212:215], v[124:127]
	v_mfma_f32_16x16x32_bf16 v[128:131], v[232:235], v[200:203], v[128:131]
	v_mfma_f32_16x16x32_bf16 v[132:135], v[232:235], v[204:207], v[132:135]
	v_mfma_f32_16x16x32_bf16 v[136:139], v[232:235], v[208:211], v[136:139]
	v_mfma_f32_16x16x32_bf16 v[140:143], v[232:235], v[212:215], v[140:143]
	v_mfma_f32_16x16x32_bf16 v[144:147], v[236:239], v[200:203], v[144:147]
	v_mfma_f32_16x16x32_bf16 v[148:151], v[236:239], v[204:207], v[148:151]
	v_mfma_f32_16x16x32_bf16 v[152:155], v[236:239], v[208:211], v[152:155]
	v_mfma_f32_16x16x32_bf16 v[156:159], v[236:239], v[212:215], v[156:159]
	s_waitcnt lgkmcnt(0)
	v_mfma_f32_16x16x32_bf16 v[64:67], v[176:179], v[160:163], v[64:67]
	ds_read_b128 v[200:203], v11 offset:0
	v_mfma_f32_16x16x32_bf16 v[68:71], v[176:179], v[164:167], v[68:71]
	ds_read_b128 v[204:207], v11 offset:2048
	v_mfma_f32_16x16x32_bf16 v[72:75], v[176:179], v[168:171], v[72:75]
	ds_read_b128 v[208:211], v11 offset:4096
	v_mfma_f32_16x16x32_bf16 v[76:79], v[176:179], v[172:175], v[76:79]
	ds_read_b128 v[212:215], v11 offset:6144
	v_mfma_f32_16x16x32_bf16 v[80:83], v[180:183], v[160:163], v[80:83]
	ds_read_b128 v[216:219], v13 offset:0
	v_mfma_f32_16x16x32_bf16 v[84:87], v[180:183], v[164:167], v[84:87]
	ds_read_b128 v[220:223], v13 offset:2048
	v_mfma_f32_16x16x32_bf16 v[88:91], v[180:183], v[168:171], v[88:91]
	ds_read_b128 v[224:227], v13 offset:4096
	v_mfma_f32_16x16x32_bf16 v[92:95], v[180:183], v[172:175], v[92:95]
	ds_read_b128 v[228:231], v13 offset:6144
	v_mfma_f32_16x16x32_bf16 v[96:99], v[184:187], v[160:163], v[96:99]
	ds_read_b128 v[232:235], v13 offset:8192
	v_mfma_f32_16x16x32_bf16 v[100:103], v[184:187], v[164:167], v[100:103]
	ds_read_b128 v[236:239], v13 offset:10240
	v_mfma_f32_16x16x32_bf16 v[104:107], v[184:187], v[168:171], v[104:107]
	v_mfma_f32_16x16x32_bf16 v[108:111], v[184:187], v[172:175], v[108:111]
	v_mfma_f32_16x16x32_bf16 v[112:115], v[188:191], v[160:163], v[112:115]
	v_mfma_f32_16x16x32_bf16 v[116:119], v[188:191], v[164:167], v[116:119]
	v_mfma_f32_16x16x32_bf16 v[120:123], v[188:191], v[168:171], v[120:123]
	v_mfma_f32_16x16x32_bf16 v[124:127], v[188:191], v[172:175], v[124:127]
	v_mfma_f32_16x16x32_bf16 v[128:131], v[192:195], v[160:163], v[128:131]
	v_mfma_f32_16x16x32_bf16 v[132:135], v[192:195], v[164:167], v[132:135]
	v_mfma_f32_16x16x32_bf16 v[136:139], v[192:195], v[168:171], v[136:139]
	v_mfma_f32_16x16x32_bf16 v[140:143], v[192:195], v[172:175], v[140:143]
	v_mfma_f32_16x16x32_bf16 v[144:147], v[196:199], v[160:163], v[144:147]
	v_add_u32_e32 v10, s21, v8
	v_add_u32_e32 v12, s21, v9
	v_xor_b32_e32 v11, 64, v10
	v_xor_b32_e32 v13, 64, v12
	v_mfma_f32_16x16x32_bf16 v[148:151], v[196:199], v[164:167], v[148:151]
	s_add_u32 s21, s21, 0xa000
	s_sub_u32 s23, s21, 0x28000
	s_cmp_ge_u32 s21, 0x28000
	s_cselect_b32 s21, s23, s21
	v_mfma_f32_16x16x32_bf16 v[152:155], v[196:199], v[168:171], v[152:155]
	v_mfma_f32_16x16x32_bf16 v[156:159], v[196:199], v[172:175], v[156:159]
	s_waitcnt vmcnt(10) lgkmcnt(0)
	s_barrier
	v_mfma_f32_16x16x32_bf16 v[64:67], v[216:219], v[200:203], v[64:67]
	ds_read_b128 v[160:163], v10 offset:0
	v_mfma_f32_16x16x32_bf16 v[68:71], v[216:219], v[204:207], v[68:71]
	ds_read_b128 v[164:167], v10 offset:2048
	v_mfma_f32_16x16x32_bf16 v[72:75], v[216:219], v[208:211], v[72:75]
	ds_read_b128 v[168:171], v10 offset:4096
	v_mfma_f32_16x16x32_bf16 v[76:79], v[216:219], v[212:215], v[76:79]
	ds_read_b128 v[172:175], v10 offset:6144
	v_mfma_f32_16x16x32_bf16 v[80:83], v[220:223], v[200:203], v[80:83]
	ds_read_b128 v[176:179], v12 offset:0
	v_mfma_f32_16x16x32_bf16 v[84:87], v[220:223], v[204:207], v[84:87]
	ds_read_b128 v[180:183], v12 offset:2048
	v_mfma_f32_16x16x32_bf16 v[88:91], v[220:223], v[208:211], v[88:91]
	ds_read_b128 v[184:187], v12 offset:4096
	v_mfma_f32_16x16x32_bf16 v[92:95], v[220:223], v[212:215], v[92:95]
	ds_read_b128 v[188:191], v12 offset:6144
	v_mfma_f32_16x16x32_bf16 v[96:99], v[224:227], v[200:203], v[96:99]
	ds_read_b128 v[192:195], v12 offset:8192
	v_mfma_f32_16x16x32_bf16 v[100:103], v[224:227], v[204:207], v[100:103]
	ds_read_b128 v[196:199], v12 offset:10240
	v_mfma_f32_16x16x32_bf16 v[104:107], v[224:227], v[208:211], v[104:107]
	v_mfma_f32_16x16x32_bf16 v[108:111], v[224:227], v[212:215], v[108:111]
	v_mfma_f32_16x16x32_bf16 v[112:115], v[228:231], v[200:203], v[112:115]
	v_mfma_f32_16x16x32_bf16 v[116:119], v[228:231], v[204:207], v[116:119]
	v_mfma_f32_16x16x32_bf16 v[120:123], v[228:231], v[208:211], v[120:123]
	v_mfma_f32_16x16x32_bf16 v[124:127], v[228:231], v[212:215], v[124:127]
	v_mfma_f32_16x16x32_bf16 v[128:131], v[232:235], v[200:203], v[128:131]
	v_mfma_f32_16x16x32_bf16 v[132:135], v[232:235], v[204:207], v[132:135]
	v_mfma_f32_16x16x32_bf16 v[136:139], v[232:235], v[208:211], v[136:139]
	v_mfma_f32_16x16x32_bf16 v[140:143], v[232:235], v[212:215], v[140:143]
	v_mfma_f32_16x16x32_bf16 v[144:147], v[236:239], v[200:203], v[144:147]
	v_mfma_f32_16x16x32_bf16 v[148:151], v[236:239], v[204:207], v[148:151]
	v_mfma_f32_16x16x32_bf16 v[152:155], v[236:239], v[208:211], v[152:155]
	v_mfma_f32_16x16x32_bf16 v[156:159], v[236:239], v[212:215], v[156:159]
	s_waitcnt lgkmcnt(0)
	v_mfma_f32_16x16x32_bf16 v[64:67], v[176:179], v[160:163], v[64:67]
	ds_read_b128 v[200:203], v11 offset:0
	v_mfma_f32_16x16x32_bf16 v[68:71], v[176:179], v[164:167], v[68:71]
	ds_read_b128 v[204:207], v11 offset:2048
	v_mfma_f32_16x16x32_bf16 v[72:75], v[176:179], v[168:171], v[72:75]
	ds_read_b128 v[208:211], v11 offset:4096
	v_mfma_f32_16x16x32_bf16 v[76:79], v[176:179], v[172:175], v[76:79]
	ds_read_b128 v[212:215], v11 offset:6144
	v_mfma_f32_16x16x32_bf16 v[80:83], v[180:183], v[160:163], v[80:83]
	ds_read_b128 v[216:219], v13 offset:0
	v_mfma_f32_16x16x32_bf16 v[84:87], v[180:183], v[164:167], v[84:87]
	ds_read_b128 v[220:223], v13 offset:2048
	v_mfma_f32_16x16x32_bf16 v[88:91], v[180:183], v[168:171], v[88:91]
	ds_read_b128 v[224:227], v13 offset:4096
	v_mfma_f32_16x16x32_bf16 v[92:95], v[180:183], v[172:175], v[92:95]
	ds_read_b128 v[228:231], v13 offset:6144
	v_mfma_f32_16x16x32_bf16 v[96:99], v[184:187], v[160:163], v[96:99]
	ds_read_b128 v[232:235], v13 offset:8192
	v_mfma_f32_16x16x32_bf16 v[100:103], v[184:187], v[164:167], v[100:103]
	ds_read_b128 v[236:239], v13 offset:10240
	v_mfma_f32_16x16x32_bf16 v[104:107], v[184:187], v[168:171], v[104:107]
	v_mfma_f32_16x16x32_bf16 v[108:111], v[184:187], v[172:175], v[108:111]
	v_mfma_f32_16x16x32_bf16 v[112:115], v[188:191], v[160:163], v[112:115]
	v_mfma_f32_16x16x32_bf16 v[116:119], v[188:191], v[164:167], v[116:119]
	v_mfma_f32_16x16x32_bf16 v[120:123], v[188:191], v[168:171], v[120:123]
	v_mfma_f32_16x16x32_bf16 v[124:127], v[188:191], v[172:175], v[124:127]
	v_mfma_f32_16x16x32_bf16 v[128:131], v[192:195], v[160:163], v[128:131]
	v_mfma_f32_16x16x32_bf16 v[132:135], v[192:195], v[164:167], v[132:135]
	v_mfma_f32_16x16x32_bf16 v[136:139], v[192:195], v[168:171], v[136:139]
	v_mfma_f32_16x16x32_bf16 v[140:143], v[192:195], v[172:175], v[140:143]
	v_mfma_f32_16x16x32_bf16 v[144:147], v[196:199], v[160:163], v[144:147]
	v_add_u32_e32 v10, s21, v8
	v_add_u32_e32 v12, s21, v9
	v_xor_b32_e32 v11, 64, v10
	v_xor_b32_e32 v13, 64, v12
	v_mfma_f32_16x16x32_bf16 v[148:151], v[196:199], v[164:167], v[148:151]
	s_add_u32 s21, s21, 0xa000
	s_sub_u32 s23, s21, 0x28000
	s_cmp_ge_u32 s21, 0x28000
	s_cselect_b32 s21, s23, s21
	v_mfma_f32_16x16x32_bf16 v[152:155], v[196:199], v[168:171], v[152:155]
	v_mfma_f32_16x16x32_bf16 v[156:159], v[196:199], v[172:175], v[156:159]
	s_waitcnt vmcnt(0) lgkmcnt(0)
	s_barrier
	v_mfma_f32_16x16x32_bf16 v[64:67], v[216:219], v[200:203], v[64:67]
	ds_read_b128 v[160:163], v10 offset:0
	v_mfma_f32_16x16x32_bf16 v[68:71], v[216:219], v[204:207], v[68:71]
	global_load_dwordx4 v[16:19], v56, s[8:9] offset:0
	v_mfma_f32_16x16x32_bf16 v[72:75], v[216:219], v[208:211], v[72:75]
	ds_read_b128 v[164:167], v10 offset:2048
	v_mfma_f32_16x16x32_bf16 v[76:79], v[216:219], v[212:215], v[76:79]
	global_load_dwordx4 v[20:23], v57, s[8:9] offset:0
	v_mfma_f32_16x16x32_bf16 v[80:83], v[220:223], v[200:203], v[80:83]
	ds_read_b128 v[168:171], v10 offset:4096
	v_mfma_f32_16x16x32_bf16 v[84:87], v[220:223], v[204:207], v[84:87]
	global_load_dwordx4 v[24:27], v58, s[8:9] offset:0
	v_mfma_f32_16x16x32_bf16 v[88:91], v[220:223], v[208:211], v[88:91]
	ds_read_b128 v[172:175], v10 offset:6144
	v_mfma_f32_16x16x32_bf16 v[92:95], v[220:223], v[212:215], v[92:95]
	global_load_dwordx4 v[28:31], v59, s[8:9] offset:0
	v_mfma_f32_16x16x32_bf16 v[96:99], v[224:227], v[200:203], v[96:99]
	ds_read_b128 v[176:179], v12 offset:0
	v_mfma_f32_16x16x32_bf16 v[100:103], v[224:227], v[204:207], v[100:103]
	global_load_dwordx4 v[32:35], v56, s[8:9] offset:64
	v_mfma_f32_16x16x32_bf16 v[104:107], v[224:227], v[208:211], v[104:107]
	ds_read_b128 v[180:183], v12 offset:2048
	v_mfma_f32_16x16x32_bf16 v[108:111], v[224:227], v[212:215], v[108:111]
	global_load_dwordx4 v[36:39], v57, s[8:9] offset:64
	v_mfma_f32_16x16x32_bf16 v[112:115], v[228:231], v[200:203], v[112:115]
	ds_read_b128 v[184:187], v12 offset:4096
	v_mfma_f32_16x16x32_bf16 v[116:119], v[228:231], v[204:207], v[116:119]
	global_load_dwordx4 v[40:43], v58, s[8:9] offset:64
	v_mfma_f32_16x16x32_bf16 v[120:123], v[228:231], v[208:211], v[120:123]
	ds_read_b128 v[188:191], v12 offset:6144
	v_mfma_f32_16x16x32_bf16 v[124:127], v[228:231], v[212:215], v[124:127]
	global_load_dwordx4 v[44:47], v59, s[8:9] offset:64
	v_mfma_f32_16x16x32_bf16 v[128:131], v[232:235], v[200:203], v[128:131]
	ds_read_b128 v[192:195], v12 offset:8192
	v_mfma_f32_16x16x32_bf16 v[132:135], v[232:235], v[204:207], v[132:135]
	global_load_dwordx4 v[48:51], v56, s[8:9] offset:128
	v_mfma_f32_16x16x32_bf16 v[136:139], v[232:235], v[208:211], v[136:139]
	ds_read_b128 v[196:199], v12 offset:10240
	v_mfma_f32_16x16x32_bf16 v[140:143], v[232:235], v[212:215], v[140:143]
	global_load_dwordx4 v[52:55], v57, s[8:9] offset:128
	v_mfma_f32_16x16x32_bf16 v[144:147], v[236:239], v[200:203], v[144:147]
	global_load_dwordx4 v[240:243], v58, s[8:9] offset:128
	v_mfma_f32_16x16x32_bf16 v[148:151], v[236:239], v[204:207], v[148:151]
	global_load_dwordx4 v[244:247], v59, s[8:9] offset:128
	v_mfma_f32_16x16x32_bf16 v[152:155], v[236:239], v[208:211], v[152:155]
	global_load_dwordx4 v[248:251], v56, s[8:9] offset:192
	v_mfma_f32_16x16x32_bf16 v[156:159], v[236:239], v[212:215], v[156:159]
	global_load_dwordx4 v[252:255], v57, s[8:9] offset:192
	s_waitcnt lgkmcnt(0)
	v_mfma_f32_16x16x32_bf16 v[64:67], v[176:179], v[160:163], v[64:67]
	ds_read_b128 v[200:203], v11 offset:0
	v_mfma_f32_16x16x32_bf16 v[68:71], v[176:179], v[164:167], v[68:71]
	ds_read_b128 v[204:207], v11 offset:2048
	v_mfma_f32_16x16x32_bf16 v[72:75], v[176:179], v[168:171], v[72:75]
	ds_read_b128 v[208:211], v11 offset:4096
	v_mfma_f32_16x16x32_bf16 v[76:79], v[176:179], v[172:175], v[76:79]
	ds_read_b128 v[212:215], v11 offset:6144
	v_mfma_f32_16x16x32_bf16 v[80:83], v[180:183], v[160:163], v[80:83]
	ds_read_b128 v[216:219], v13 offset:0
	v_mfma_f32_16x16x32_bf16 v[84:87], v[180:183], v[164:167], v[84:87]
	ds_read_b128 v[220:223], v13 offset:2048
	v_mfma_f32_16x16x32_bf16 v[88:91], v[180:183], v[168:171], v[88:91]
	ds_read_b128 v[224:227], v13 offset:4096
	v_mfma_f32_16x16x32_bf16 v[92:95], v[180:183], v[172:175], v[92:95]
	ds_read_b128 v[228:231], v13 offset:6144
	v_mfma_f32_16x16x32_bf16 v[96:99], v[184:187], v[160:163], v[96:99]
	ds_read_b128 v[232:235], v13 offset:8192
	v_mfma_f32_16x16x32_bf16 v[100:103], v[184:187], v[164:167], v[100:103]
	ds_read_b128 v[236:239], v13 offset:10240
	v_mfma_f32_16x16x32_bf16 v[104:107], v[184:187], v[168:171], v[104:107]
	v_mfma_f32_16x16x32_bf16 v[108:111], v[184:187], v[172:175], v[108:111]
	v_mfma_f32_16x16x32_bf16 v[112:115], v[188:191], v[160:163], v[112:115]
	v_mfma_f32_16x16x32_bf16 v[116:119], v[188:191], v[164:167], v[116:119]
	v_mfma_f32_16x16x32_bf16 v[120:123], v[188:191], v[168:171], v[120:123]
	v_mfma_f32_16x16x32_bf16 v[124:127], v[188:191], v[172:175], v[124:127]
	v_mfma_f32_16x16x32_bf16 v[128:131], v[192:195], v[160:163], v[128:131]
	v_mfma_f32_16x16x32_bf16 v[132:135], v[192:195], v[164:167], v[132:135]
	v_mfma_f32_16x16x32_bf16 v[136:139], v[192:195], v[168:171], v[136:139]
	v_mfma_f32_16x16x32_bf16 v[140:143], v[192:195], v[172:175], v[140:143]
	v_mfma_f32_16x16x32_bf16 v[144:147], v[196:199], v[160:163], v[144:147]
	v_mfma_f32_16x16x32_bf16 v[148:151], v[196:199], v[164:167], v[148:151]
	v_mfma_f32_16x16x32_bf16 v[152:155], v[196:199], v[168:171], v[152:155]
	v_mfma_f32_16x16x32_bf16 v[156:159], v[196:199], v[172:175], v[156:159]
	s_waitcnt lgkmcnt(0)
	v_mfma_f32_16x16x32_bf16 v[64:67], v[216:219], v[200:203], v[64:67]
	v_mfma_f32_16x16x32_bf16 v[68:71], v[216:219], v[204:207], v[68:71]
	global_load_dwordx4 v[160:163], v58, s[8:9] offset:192
	v_mfma_f32_16x16x32_bf16 v[72:75], v[216:219], v[208:211], v[72:75]
	v_mfma_f32_16x16x32_bf16 v[76:79], v[216:219], v[212:215], v[76:79]
	global_load_dwordx4 v[164:167], v59, s[8:9] offset:192
	v_mfma_f32_16x16x32_bf16 v[80:83], v[220:223], v[200:203], v[80:83]
	v_mfma_f32_16x16x32_bf16 v[84:87], v[220:223], v[204:207], v[84:87]
	global_load_dwordx4 v[168:171], v56, s[8:9] offset:256
	v_mfma_f32_16x16x32_bf16 v[88:91], v[220:223], v[208:211], v[88:91]
	v_mfma_f32_16x16x32_bf16 v[92:95], v[220:223], v[212:215], v[92:95]
	global_load_dwordx4 v[172:175], v57, s[8:9] offset:256
	v_mfma_f32_16x16x32_bf16 v[96:99], v[224:227], v[200:203], v[96:99]
	v_mfma_f32_16x16x32_bf16 v[100:103], v[224:227], v[204:207], v[100:103]
	global_load_dwordx4 v[176:179], v58, s[8:9] offset:256
	v_mfma_f32_16x16x32_bf16 v[104:107], v[224:227], v[208:211], v[104:107]
	v_mfma_f32_16x16x32_bf16 v[108:111], v[224:227], v[212:215], v[108:111]
	global_load_dwordx4 v[180:183], v59, s[8:9] offset:256
	v_mfma_f32_16x16x32_bf16 v[112:115], v[228:231], v[200:203], v[112:115]
	v_mfma_f32_16x16x32_bf16 v[116:119], v[228:231], v[204:207], v[116:119]
	global_load_dwordx4 v[184:187], v56, s[8:9] offset:320
	v_mfma_f32_16x16x32_bf16 v[120:123], v[228:231], v[208:211], v[120:123]
	v_mfma_f32_16x16x32_bf16 v[124:127], v[228:231], v[212:215], v[124:127]
	global_load_dwordx4 v[188:191], v57, s[8:9] offset:320
	v_mfma_f32_16x16x32_bf16 v[128:131], v[232:235], v[200:203], v[128:131]
	v_mfma_f32_16x16x32_bf16 v[132:135], v[232:235], v[204:207], v[132:135]
	global_load_dwordx4 v[192:195], v58, s[8:9] offset:320
	v_mfma_f32_16x16x32_bf16 v[136:139], v[232:235], v[208:211], v[136:139]
	v_mfma_f32_16x16x32_bf16 v[140:143], v[232:235], v[212:215], v[140:143]
	global_load_dwordx4 v[196:199], v59, s[8:9] offset:320
	v_mfma_f32_16x16x32_bf16 v[144:147], v[236:239], v[200:203], v[144:147]
	v_mfma_f32_16x16x32_bf16 v[148:151], v[236:239], v[204:207], v[148:151]
	v_mfma_f32_16x16x32_bf16 v[152:155], v[236:239], v[208:211], v[152:155]
	v_mfma_f32_16x16x32_bf16 v[156:159], v[236:239], v[212:215], v[156:159]
	v_and_b32_e32 v12, 63, v0
	v_cmp_gt_u32_e32 vcc, 16, v12
	v_xor_b32_e32 v13, 16, v12
	v_lshlrev_b32_e32 v13, 2, v13
	v_xor_b32_e32 v12, 32, v12
	v_lshlrev_b32_e32 v12, 2, v12
	v_bfe_u32 v14, v0, 6, 1
	v_mul_u32_u24_e32 v14, 0x60, v14
	v_bfe_u32 v15, v0, 4, 2
	v_lshl_add_u32 v14, v15, 2, v14
	v_add_u32_e32 v14, s13, v14
	v_lshlrev_b32_e32 v14, 2, v14
	global_load_dwordx4 v[200:203], v14, s[24:25]
	global_load_dwordx4 v[204:207], v14, s[24:25] offset:64
	global_load_dwordx4 v[208:211], v14, s[24:25] offset:128
	global_load_dwordx4 v[212:215], v14, s[24:25] offset:192
	global_load_dwordx4 v[216:219], v14, s[24:25] offset:256
	global_load_dwordx4 v[220:223], v14, s[24:25] offset:320
	v_lshrrev_b32_e32 v60, 1, v56
	v_lshrrev_b32_e32 v61, 1, v57
	v_lshrrev_b32_e32 v62, 1, v58
	v_lshrrev_b32_e32 v63, 1, v59
	v_bfe_u32 v8, v0, 7, 1
	v_and_b32_e32 v9, 15, v0
	v_lshl_add_u32 v8, v8, 6, v9
	v_add_u32_e32 v8, s12, v8
	v_lshlrev_b32_e32 v8, 6, v8
	v_bfe_u32 v9, v0, 6, 1
	v_lshlrev_b32_e32 v9, 1, v9
	v_add_u32_e32 v9, s30, v9
	v_lshl_add_u32 v8, v9, 2, v8
	v_add_u32_e32 v9, 0x400, v8
	v_add_u32_e32 v10, 0x400, v9
	v_add_u32_e32 v11, 0x400, v10
	s_waitcnt vmcnt(0)
	v_pk_add_f32 v[64:65], v[64:65], v[16:17]
	v_pk_add_f32 v[66:67], v[66:67], v[18:19]
	global_store_dwordx4 v56, v[64:67], s[10:11]
	v_pk_mul_f32 v[224:225], v[200:201], v[64:65]
	v_pk_mul_f32 v[226:227], v[202:203], v[66:67]
	v_cvt_pk_bf16_f32 v228, v224, v225
	v_cvt_pk_bf16_f32 v229, v226, v227
	global_store_dwordx2 v60, v[228:229], s[28:29]
	v_pk_mul_f32 v[230:231], v[64:65], v[64:65]
	v_pk_mul_f32 v[232:233], v[66:67], v[66:67]
	v_add_f32_e32 v230, v230, v231
	v_add_f32_e32 v230, v232, v230
	v_add_f32_e32 v234, v233, v230
	v_pk_add_f32 v[80:81], v[80:81], v[32:33]
	v_pk_add_f32 v[82:83], v[82:83], v[34:35]
	global_store_dwordx4 v56, v[80:83], s[10:11] offset:64
	v_pk_mul_f32 v[224:225], v[204:205], v[80:81]
	v_pk_mul_f32 v[226:227], v[206:207], v[82:83]
	v_cvt_pk_bf16_f32 v228, v224, v225
	v_cvt_pk_bf16_f32 v229, v226, v227
	global_store_dwordx2 v60, v[228:229], s[28:29] offset:32
	v_pk_mul_f32 v[230:231], v[80:81], v[80:81]
	v_pk_mul_f32 v[232:233], v[82:83], v[82:83]
	v_add_f32_e32 v230, v230, v231
	v_add_f32_e32 v230, v232, v230
	v_add_f32_e32 v230, v233, v230
	v_add_f32_e32 v234, v234, v230
	v_pk_add_f32 v[96:97], v[96:97], v[48:49]
	v_pk_add_f32 v[98:99], v[98:99], v[50:51]
	global_store_dwordx4 v56, v[96:99], s[10:11] offset:128
	v_pk_mul_f32 v[224:225], v[208:209], v[96:97]
	v_pk_mul_f32 v[226:227], v[210:211], v[98:99]
	v_cvt_pk_bf16_f32 v228, v224, v225
	v_cvt_pk_bf16_f32 v229, v226, v227
	global_store_dwordx2 v60, v[228:229], s[28:29] offset:64
	v_pk_mul_f32 v[230:231], v[96:97], v[96:97]
	v_pk_mul_f32 v[232:233], v[98:99], v[98:99]
	v_add_f32_e32 v230, v230, v231
	v_add_f32_e32 v230, v232, v230
	v_add_f32_e32 v230, v233, v230
	v_add_f32_e32 v234, v234, v230
	v_pk_add_f32 v[112:113], v[112:113], v[248:249]
	v_pk_add_f32 v[114:115], v[114:115], v[250:251]
	global_store_dwordx4 v56, v[112:115], s[10:11] offset:192
	v_pk_mul_f32 v[224:225], v[212:213], v[112:113]
	v_pk_mul_f32 v[226:227], v[214:215], v[114:115]
	v_cvt_pk_bf16_f32 v228, v224, v225
	v_cvt_pk_bf16_f32 v229, v226, v227
	global_store_dwordx2 v60, v[228:229], s[28:29] offset:96
	v_pk_mul_f32 v[230:231], v[112:113], v[112:113]
	v_pk_mul_f32 v[232:233], v[114:115], v[114:115]
	v_add_f32_e32 v230, v230, v231
	v_add_f32_e32 v230, v232, v230
	v_add_f32_e32 v235, v233, v230
	v_pk_add_f32 v[128:129], v[128:129], v[168:169]
	v_pk_add_f32 v[130:131], v[130:131], v[170:171]
	global_store_dwordx4 v56, v[128:131], s[10:11] offset:256
	v_pk_mul_f32 v[224:225], v[216:217], v[128:129]
	v_pk_mul_f32 v[226:227], v[218:219], v[130:131]
	v_cvt_pk_bf16_f32 v228, v224, v225
	v_cvt_pk_bf16_f32 v229, v226, v227
	global_store_dwordx2 v60, v[228:229], s[28:29] offset:128
	v_pk_mul_f32 v[230:231], v[128:129], v[128:129]
	v_pk_mul_f32 v[232:233], v[130:131], v[130:131]
	v_add_f32_e32 v230, v230, v231
	v_add_f32_e32 v230, v232, v230
	v_add_f32_e32 v230, v233, v230
	v_add_f32_e32 v235, v235, v230
	v_pk_add_f32 v[144:145], v[144:145], v[184:185]
	v_pk_add_f32 v[146:147], v[146:147], v[186:187]
	global_store_dwordx4 v56, v[144:147], s[10:11] offset:320
	v_pk_mul_f32 v[224:225], v[220:221], v[144:145]
	v_pk_mul_f32 v[226:227], v[222:223], v[146:147]
	v_cvt_pk_bf16_f32 v228, v224, v225
	v_cvt_pk_bf16_f32 v229, v226, v227
	global_store_dwordx2 v60, v[228:229], s[28:29] offset:160
	v_pk_mul_f32 v[230:231], v[144:145], v[144:145]
	v_pk_mul_f32 v[232:233], v[146:147], v[146:147]
	v_add_f32_e32 v230, v230, v231
	v_add_f32_e32 v230, v232, v230
	v_add_f32_e32 v230, v233, v230
	v_add_f32_e32 v235, v235, v230
	v_pk_add_f32 v[68:69], v[68:69], v[20:21]
	v_pk_add_f32 v[70:71], v[70:71], v[22:23]
	global_store_dwordx4 v57, v[68:71], s[10:11]
	v_pk_mul_f32 v[224:225], v[200:201], v[68:69]
	v_pk_mul_f32 v[226:227], v[202:203], v[70:71]
	v_cvt_pk_bf16_f32 v228, v224, v225
	v_cvt_pk_bf16_f32 v229, v226, v227
	global_store_dwordx2 v61, v[228:229], s[28:29]
	v_pk_mul_f32 v[230:231], v[68:69], v[68:69]
	v_pk_mul_f32 v[232:233], v[70:71], v[70:71]
	v_add_f32_e32 v230, v230, v231
	v_add_f32_e32 v230, v232, v230
	v_add_f32_e32 v236, v233, v230
	v_pk_add_f32 v[84:85], v[84:85], v[36:37]
	v_pk_add_f32 v[86:87], v[86:87], v[38:39]
	global_store_dwordx4 v57, v[84:87], s[10:11] offset:64
	v_pk_mul_f32 v[224:225], v[204:205], v[84:85]
	v_pk_mul_f32 v[226:227], v[206:207], v[86:87]
	v_cvt_pk_bf16_f32 v228, v224, v225
	v_cvt_pk_bf16_f32 v229, v226, v227
	global_store_dwordx2 v61, v[228:229], s[28:29] offset:32
	v_pk_mul_f32 v[230:231], v[84:85], v[84:85]
	v_pk_mul_f32 v[232:233], v[86:87], v[86:87]
	v_add_f32_e32 v230, v230, v231
	v_add_f32_e32 v230, v232, v230
	v_add_f32_e32 v230, v233, v230
	v_add_f32_e32 v236, v236, v230
	v_pk_add_f32 v[100:101], v[100:101], v[52:53]
	v_pk_add_f32 v[102:103], v[102:103], v[54:55]
	global_store_dwordx4 v57, v[100:103], s[10:11] offset:128
	v_pk_mul_f32 v[224:225], v[208:209], v[100:101]
	v_pk_mul_f32 v[226:227], v[210:211], v[102:103]
	v_cvt_pk_bf16_f32 v228, v224, v225
	v_cvt_pk_bf16_f32 v229, v226, v227
	global_store_dwordx2 v61, v[228:229], s[28:29] offset:64
	v_pk_mul_f32 v[230:231], v[100:101], v[100:101]
	v_pk_mul_f32 v[232:233], v[102:103], v[102:103]
	v_add_f32_e32 v230, v230, v231
	v_add_f32_e32 v230, v232, v230
	v_add_f32_e32 v230, v233, v230
	v_add_f32_e32 v236, v236, v230
	v_pk_add_f32 v[116:117], v[116:117], v[252:253]
	v_pk_add_f32 v[118:119], v[118:119], v[254:255]
	global_store_dwordx4 v57, v[116:119], s[10:11] offset:192
	v_pk_mul_f32 v[224:225], v[212:213], v[116:117]
	v_pk_mul_f32 v[226:227], v[214:215], v[118:119]
	v_cvt_pk_bf16_f32 v228, v224, v225
	v_cvt_pk_bf16_f32 v229, v226, v227
	global_store_dwordx2 v61, v[228:229], s[28:29] offset:96
	v_pk_mul_f32 v[230:231], v[116:117], v[116:117]
	v_pk_mul_f32 v[232:233], v[118:119], v[118:119]
	v_add_f32_e32 v230, v230, v231
	v_add_f32_e32 v230, v232, v230
	v_add_f32_e32 v237, v233, v230
	v_pk_add_f32 v[132:133], v[132:133], v[172:173]
	v_pk_add_f32 v[134:135], v[134:135], v[174:175]
	global_store_dwordx4 v57, v[132:135], s[10:11] offset:256
	v_pk_mul_f32 v[224:225], v[216:217], v[132:133]
	v_pk_mul_f32 v[226:227], v[218:219], v[134:135]
	v_cvt_pk_bf16_f32 v228, v224, v225
	v_cvt_pk_bf16_f32 v229, v226, v227
	global_store_dwordx2 v61, v[228:229], s[28:29] offset:128
	v_pk_mul_f32 v[230:231], v[132:133], v[132:133]
	v_pk_mul_f32 v[232:233], v[134:135], v[134:135]
	v_add_f32_e32 v230, v230, v231
	v_add_f32_e32 v230, v232, v230
	v_add_f32_e32 v230, v233, v230
	v_add_f32_e32 v237, v237, v230
	v_pk_add_f32 v[148:149], v[148:149], v[188:189]
	v_pk_add_f32 v[150:151], v[150:151], v[190:191]
	global_store_dwordx4 v57, v[148:151], s[10:11] offset:320
	v_pk_mul_f32 v[224:225], v[220:221], v[148:149]
	v_pk_mul_f32 v[226:227], v[222:223], v[150:151]
	v_cvt_pk_bf16_f32 v228, v224, v225
	v_cvt_pk_bf16_f32 v229, v226, v227
	global_store_dwordx2 v61, v[228:229], s[28:29] offset:160
	v_pk_mul_f32 v[230:231], v[148:149], v[148:149]
	v_pk_mul_f32 v[232:233], v[150:151], v[150:151]
	v_add_f32_e32 v230, v230, v231
	v_add_f32_e32 v230, v232, v230
	v_add_f32_e32 v230, v233, v230
	v_add_f32_e32 v237, v237, v230
	v_pk_add_f32 v[72:73], v[72:73], v[24:25]
	v_pk_add_f32 v[74:75], v[74:75], v[26:27]
	global_store_dwordx4 v58, v[72:75], s[10:11]
	v_pk_mul_f32 v[224:225], v[200:201], v[72:73]
	v_pk_mul_f32 v[226:227], v[202:203], v[74:75]
	v_cvt_pk_bf16_f32 v228, v224, v225
	v_cvt_pk_bf16_f32 v229, v226, v227
	global_store_dwordx2 v62, v[228:229], s[28:29]
	v_pk_mul_f32 v[230:231], v[72:73], v[72:73]
	v_pk_mul_f32 v[232:233], v[74:75], v[74:75]
	v_add_f32_e32 v230, v230, v231
	v_add_f32_e32 v230, v232, v230
	v_add_f32_e32 v238, v233, v230
	v_pk_add_f32 v[88:89], v[88:89], v[40:41]
	v_pk_add_f32 v[90:91], v[90:91], v[42:43]
	global_store_dwordx4 v58, v[88:91], s[10:11] offset:64
	v_pk_mul_f32 v[224:225], v[204:205], v[88:89]
	v_pk_mul_f32 v[226:227], v[206:207], v[90:91]
	v_cvt_pk_bf16_f32 v228, v224, v225
	v_cvt_pk_bf16_f32 v229, v226, v227
	global_store_dwordx2 v62, v[228:229], s[28:29] offset:32
	v_pk_mul_f32 v[230:231], v[88:89], v[88:89]
	v_pk_mul_f32 v[232:233], v[90:91], v[90:91]
	v_add_f32_e32 v230, v230, v231
	v_add_f32_e32 v230, v232, v230
	v_add_f32_e32 v230, v233, v230
	v_add_f32_e32 v238, v238, v230
	v_pk_add_f32 v[104:105], v[104:105], v[240:241]
	v_pk_add_f32 v[106:107], v[106:107], v[242:243]
	global_store_dwordx4 v58, v[104:107], s[10:11] offset:128
	v_pk_mul_f32 v[224:225], v[208:209], v[104:105]
	v_pk_mul_f32 v[226:227], v[210:211], v[106:107]
	v_cvt_pk_bf16_f32 v228, v224, v225
	v_cvt_pk_bf16_f32 v229, v226, v227
	global_store_dwordx2 v62, v[228:229], s[28:29] offset:64
	v_pk_mul_f32 v[230:231], v[104:105], v[104:105]
	v_pk_mul_f32 v[232:233], v[106:107], v[106:107]
	v_add_f32_e32 v230, v230, v231
	v_add_f32_e32 v230, v232, v230
	v_add_f32_e32 v230, v233, v230
	v_add_f32_e32 v238, v238, v230
	v_pk_add_f32 v[120:121], v[120:121], v[160:161]
	v_pk_add_f32 v[122:123], v[122:123], v[162:163]
	global_store_dwordx4 v58, v[120:123], s[10:11] offset:192
	v_pk_mul_f32 v[224:225], v[212:213], v[120:121]
	v_pk_mul_f32 v[226:227], v[214:215], v[122:123]
	v_cvt_pk_bf16_f32 v228, v224, v225
	v_cvt_pk_bf16_f32 v229, v226, v227
	global_store_dwordx2 v62, v[228:229], s[28:29] offset:96
	v_pk_mul_f32 v[230:231], v[120:121], v[120:121]
	v_pk_mul_f32 v[232:233], v[122:123], v[122:123]
	v_add_f32_e32 v230, v230, v231
	v_add_f32_e32 v230, v232, v230
	v_add_f32_e32 v239, v233, v230
	v_pk_add_f32 v[136:137], v[136:137], v[176:177]
	v_pk_add_f32 v[138:139], v[138:139], v[178:179]
	global_store_dwordx4 v58, v[136:139], s[10:11] offset:256
	v_pk_mul_f32 v[224:225], v[216:217], v[136:137]
	v_pk_mul_f32 v[226:227], v[218:219], v[138:139]
	v_cvt_pk_bf16_f32 v228, v224, v225
	v_cvt_pk_bf16_f32 v229, v226, v227
	global_store_dwordx2 v62, v[228:229], s[28:29] offset:128
	v_pk_mul_f32 v[230:231], v[136:137], v[136:137]
	v_pk_mul_f32 v[232:233], v[138:139], v[138:139]
	v_add_f32_e32 v230, v230, v231
	v_add_f32_e32 v230, v232, v230
	v_add_f32_e32 v230, v233, v230
	v_add_f32_e32 v239, v239, v230
	v_pk_add_f32 v[152:153], v[152:153], v[192:193]
	v_pk_add_f32 v[154:155], v[154:155], v[194:195]
	global_store_dwordx4 v58, v[152:155], s[10:11] offset:320
	v_pk_mul_f32 v[224:225], v[220:221], v[152:153]
	v_pk_mul_f32 v[226:227], v[222:223], v[154:155]
	v_cvt_pk_bf16_f32 v228, v224, v225
	v_cvt_pk_bf16_f32 v229, v226, v227
	global_store_dwordx2 v62, v[228:229], s[28:29] offset:160
	v_pk_mul_f32 v[230:231], v[152:153], v[152:153]
	v_pk_mul_f32 v[232:233], v[154:155], v[154:155]
	v_add_f32_e32 v230, v230, v231
	v_add_f32_e32 v230, v232, v230
	v_add_f32_e32 v230, v233, v230
	v_add_f32_e32 v239, v239, v230
	v_pk_add_f32 v[76:77], v[76:77], v[28:29]
	v_pk_add_f32 v[78:79], v[78:79], v[30:31]
	global_store_dwordx4 v59, v[76:79], s[10:11]
	v_pk_mul_f32 v[224:225], v[200:201], v[76:77]
	v_pk_mul_f32 v[226:227], v[202:203], v[78:79]
	v_cvt_pk_bf16_f32 v228, v224, v225
	v_cvt_pk_bf16_f32 v229, v226, v227
	global_store_dwordx2 v63, v[228:229], s[28:29]
	v_pk_mul_f32 v[230:231], v[76:77], v[76:77]
	v_pk_mul_f32 v[232:233], v[78:79], v[78:79]
	v_add_f32_e32 v230, v230, v231
	v_add_f32_e32 v230, v232, v230
	v_add_f32_e32 v14, v233, v230
	v_pk_add_f32 v[92:93], v[92:93], v[44:45]
	v_pk_add_f32 v[94:95], v[94:95], v[46:47]
	global_store_dwordx4 v59, v[92:95], s[10:11] offset:64
	v_pk_mul_f32 v[224:225], v[204:205], v[92:93]
	v_pk_mul_f32 v[226:227], v[206:207], v[94:95]
	v_cvt_pk_bf16_f32 v228, v224, v225
	v_cvt_pk_bf16_f32 v229, v226, v227
	global_store_dwordx2 v63, v[228:229], s[28:29] offset:32
	v_pk_mul_f32 v[230:231], v[92:93], v[92:93]
	v_pk_mul_f32 v[232:233], v[94:95], v[94:95]
	v_add_f32_e32 v230, v230, v231
	v_add_f32_e32 v230, v232, v230
	v_add_f32_e32 v230, v233, v230
	v_add_f32_e32 v14, v14, v230
	v_pk_add_f32 v[108:109], v[108:109], v[244:245]
	v_pk_add_f32 v[110:111], v[110:111], v[246:247]
	global_store_dwordx4 v59, v[108:111], s[10:11] offset:128
	v_pk_mul_f32 v[224:225], v[208:209], v[108:109]
	v_pk_mul_f32 v[226:227], v[210:211], v[110:111]
	v_cvt_pk_bf16_f32 v228, v224, v225
	v_cvt_pk_bf16_f32 v229, v226, v227
	global_store_dwordx2 v63, v[228:229], s[28:29] offset:64
	v_pk_mul_f32 v[230:231], v[108:109], v[108:109]
	v_pk_mul_f32 v[232:233], v[110:111], v[110:111]
	v_add_f32_e32 v230, v230, v231
	v_add_f32_e32 v230, v232, v230
	v_add_f32_e32 v230, v233, v230
	v_add_f32_e32 v14, v14, v230
	v_pk_add_f32 v[124:125], v[124:125], v[164:165]
	v_pk_add_f32 v[126:127], v[126:127], v[166:167]
	global_store_dwordx4 v59, v[124:127], s[10:11] offset:192
	v_pk_mul_f32 v[224:225], v[212:213], v[124:125]
	v_pk_mul_f32 v[226:227], v[214:215], v[126:127]
	v_cvt_pk_bf16_f32 v228, v224, v225
	v_cvt_pk_bf16_f32 v229, v226, v227
	global_store_dwordx2 v63, v[228:229], s[28:29] offset:96
	v_pk_mul_f32 v[230:231], v[124:125], v[124:125]
	v_pk_mul_f32 v[232:233], v[126:127], v[126:127]
	v_add_f32_e32 v230, v230, v231
	v_add_f32_e32 v230, v232, v230
	v_add_f32_e32 v15, v233, v230
	v_pk_add_f32 v[140:141], v[140:141], v[180:181]
	v_pk_add_f32 v[142:143], v[142:143], v[182:183]
	global_store_dwordx4 v59, v[140:143], s[10:11] offset:256
	v_pk_mul_f32 v[224:225], v[216:217], v[140:141]
	v_pk_mul_f32 v[226:227], v[218:219], v[142:143]
	v_cvt_pk_bf16_f32 v228, v224, v225
	v_cvt_pk_bf16_f32 v229, v226, v227
	global_store_dwordx2 v63, v[228:229], s[28:29] offset:128
	v_pk_mul_f32 v[230:231], v[140:141], v[140:141]
	v_pk_mul_f32 v[232:233], v[142:143], v[142:143]
	v_add_f32_e32 v230, v230, v231
	v_add_f32_e32 v230, v232, v230
	v_add_f32_e32 v230, v233, v230
	v_add_f32_e32 v15, v15, v230
	v_pk_add_f32 v[156:157], v[156:157], v[196:197]
	v_pk_add_f32 v[158:159], v[158:159], v[198:199]
	global_store_dwordx4 v59, v[156:159], s[10:11] offset:320
	v_pk_mul_f32 v[224:225], v[220:221], v[156:157]
	v_pk_mul_f32 v[226:227], v[222:223], v[158:159]
	v_cvt_pk_bf16_f32 v228, v224, v225
	v_cvt_pk_bf16_f32 v229, v226, v227
	global_store_dwordx2 v63, v[228:229], s[28:29] offset:160
	v_pk_mul_f32 v[230:231], v[156:157], v[156:157]
	v_pk_mul_f32 v[232:233], v[158:159], v[158:159]
	v_add_f32_e32 v230, v230, v231
	v_add_f32_e32 v230, v232, v230
	v_add_f32_e32 v230, v233, v230
	v_add_f32_e32 v15, v15, v230
	ds_bpermute_b32 v224, v13, v234
	ds_bpermute_b32 v225, v13, v235
	ds_bpermute_b32 v226, v13, v236
	ds_bpermute_b32 v227, v13, v237
	ds_bpermute_b32 v228, v13, v238
	ds_bpermute_b32 v229, v13, v239
	ds_bpermute_b32 v230, v13, v14
	ds_bpermute_b32 v231, v13, v15
	s_waitcnt lgkmcnt(0)
	v_add_f32_e32 v234, v234, v224
	v_add_f32_e32 v235, v235, v225
	v_add_f32_e32 v236, v236, v226
	v_add_f32_e32 v237, v237, v227
	v_add_f32_e32 v238, v238, v228
	v_add_f32_e32 v239, v239, v229
	v_add_f32_e32 v14, v14, v230
	v_add_f32_e32 v15, v15, v231
	ds_bpermute_b32 v224, v12, v234
	ds_bpermute_b32 v225, v12, v235
	ds_bpermute_b32 v226, v12, v236
	ds_bpermute_b32 v227, v12, v237
	ds_bpermute_b32 v228, v12, v238
	ds_bpermute_b32 v229, v12, v239
	ds_bpermute_b32 v230, v12, v14
	ds_bpermute_b32 v231, v12, v15
	s_waitcnt lgkmcnt(0)
	v_add_f32_e32 v234, v234, v224
	v_add_f32_e32 v235, v235, v225
	v_add_f32_e32 v236, v236, v226
	v_add_f32_e32 v237, v237, v227
	v_add_f32_e32 v238, v238, v228
	v_add_f32_e32 v239, v239, v229
	v_add_f32_e32 v14, v14, v230
	v_add_f32_e32 v15, v15, v231
	s_and_saveexec_b64 s[2:3], vcc
	global_store_dwordx2 v8, v[234:235], s[26:27]
	global_store_dwordx2 v9, v[236:237], s[26:27]
	global_store_dwordx2 v10, v[238:239], s[26:27]
	global_store_dwordx2 v11, v[14:15], s[26:27]
	s_or_b64 exec, exec, s[2:3]
